# speedup vs baseline: 1.0948x; 1.0133x over previous
.LBB1_21:
	s_or_b64 exec, exec, s[6:7]
	s_waitcnt lgkmcnt(0)
	s_barrier
	s_cmpk_lt_u32 s3, 0x100
	s_cbranch_scc1 .Lmy_nonp6
	s_setprio 2
	s_sub_i32 s72, s42, 4
	s_lshl_b32 s72, s72, 5
	v_add_u32_e32 v1, s72, v114
	v_min_u32_e32 v2, 0x78, v1
	v_mul_u32_u24_e32 v4, 0xbb, v2
	v_lshrrev_b32_e32 v4, 11, v4
	v_mad_i32_i24 v5, v4, -11, v2
	v_sub_u32_e32 v6, 5, v4
	v_subrev_u32_e32 v7, 5, v4
	v_max_i32_e32 v6, v6, v7
	v_sub_u32_e32 v7, 5, v5
	v_subrev_u32_e32 v8, 5, v5
	v_max_i32_e32 v7, v7, v8
	v_max_i32_e32 v6, v6, v7
	v_sub_u32_e32 v7, 5, v6
	v_add_u32_e32 v8, 5, v6
	v_mul_u32_u24_e32 v9, 6, v6
	v_add_u32_e32 v9, v9, v4
	v_sub_u32_e32 v9, v9, v7
	v_lshlrev_b32_e32 v10, 2, v6
	v_add_u32_e32 v10, v10, v5
	v_sub_u32_e32 v10, v10, v7
	v_cmp_eq_u32_e32 vcc, v4, v8
	v_cmp_lt_u32_e64 s[74:75], v5, v8
	s_and_b64 vcc, vcc, s[74:75]
	v_cndmask_b32_e32 v9, v9, v10, vcc
	v_lshlrev_b32_e32 v10, 1, v6
	v_add_u32_e32 v10, v10, v4
	v_sub_u32_e32 v10, v10, v7
	v_add_u32_e32 v10, -1, v10
	v_cmp_eq_u32_e32 vcc, v5, v8
	v_cmp_gt_u32_e64 s[74:75], v4, v7
	s_and_b64 vcc, vcc, s[74:75]
	v_cndmask_b32_e32 v9, v9, v10, vcc
	v_sub_u32_e32 v10, v5, v7
	v_add_u32_e32 v10, -1, v10
	v_cmp_eq_u32_e32 vcc, v4, v7
	v_cmp_gt_u32_e64 s[74:75], v5, v7
	s_and_b64 vcc, vcc, s[74:75]
	v_cndmask_b32_e32 v9, v9, v10, vcc
	v_add_u32_e32 v10, -1, v6
	v_mul_u32_u24_e32 v10, v10, v6
	v_lshlrev_b32_e32 v10, 2, v10
	v_add3_u32 v9, v9, v10, 2
	v_cmp_ne_u32_e32 vcc, 0, v6
	s_nop 1
	v_cndmask_b32_e32 v9, 1, v9, vcc
	v_cmp_gt_u32_e32 vcc, 0x79, v1
	s_nop 1
	v_cndmask_b32_e32 v3, v1, v9, vcc
	v_cndmask_b32_e64 v12, 0, 1.0, vcc
	v_cmp_eq_u32_e32 vcc, 0x79, v1
	s_nop 1
	v_cndmask_b32_e64 v3, v3, 0, vcc
	v_cndmask_b32_e64 v14, 0, 1.0, vcc
	v_cmp_gt_u32_e32 vcc, 0x7a, v1
	s_nop 1
	v_cndmask_b32_e64 v13, 0, 1.0, vcc
	v_cmp_eq_u32_e32 vcc, 0, v115
	s_nop 1
	v_cndmask_b32_e64 v112, 52, 64, vcc
	v_min_u32_e32 v10, 0x79, v3
	v_mul_u32_u24_e32 v10, 0x54, v10
	v_lshl_add_u32 v63, v115, 4, v10
	v_add_u32_e32 v11, v63, v112
	global_load_dwordx4 v[64:67], v63, s[26:27]
	global_load_dwordx4 v[68:71], v63, s[26:27] offset:32
	global_load_dwordx4 v[72:75], v11, s[26:27]
	v_lshlrev_b32_e32 v10, 4, v115
	v_add_u32_e32 v11, v10, v112
	global_load_dwordx4 v[76:79], v10, s[28:29]
	global_load_dwordx4 v[80:83], v10, s[28:29] offset:32
	global_load_dwordx4 v[84:87], v11, s[28:29]
	v_add_u32_e32 v113, 0x12ed0, v10
	ds_read_b128 v[88:91], v113 offset:288
	ds_read_b128 v[92:95], v113 offset:320
	ds_read_b128 v[96:99], v113 offset:352
	ds_read_b128 v[100:103], v113 offset:96
	ds_read_b128 v[104:107], v113 offset:128
	ds_read_b128 v[108:111], v113 offset:160
	ds_read_b128 v[116:119], v113
	ds_read_b128 v[120:123], v113 offset:32
	ds_read_b128 v[124:127], v113 offset:64
	v_mul_u32_u24_e32 v10, 0x79, v115
	v_add_u32_e32 v10, v10, v2
	v_mul_u32_u24_e32 v60, 48, v10
	ds_read_b128 v[44:47], v60
	ds_read_b128 v[48:51], v60 offset:11616
	ds_read_b128 v[52:55], v60 offset:23232
	ds_read_b128 v[56:59], v60 offset:34848
	v_and_b32_e32 v10, 1, v114
	v_lshlrev_b32_e32 v10, 4, v10
	v_mov_b32_e32 v11, 0x3c00
	v_lshlrev_b32_e32 v61, v10, v11
	v_lshrrev_b32_e32 v62, 1, v114
	v_cmp_eq_u32_e64 s[72:73], 0, v62
	v_cmp_eq_u32_e64 s[74:75], 1, v62
	v_cmp_eq_u32_e64 s[76:77], 2, v62
	v_cmp_eq_u32_e64 s[78:79], 3, v62
	v_cmp_eq_u32_e64 s[80:81], 4, v62
	v_cmp_eq_u32_e64 s[82:83], 5, v62
	v_cmp_eq_u32_e64 s[84:85], 6, v62
	v_cmp_eq_u32_e64 s[86:87], 7, v62
	v_cmp_eq_u32_e64 s[88:89], 8, v62
	v_cmp_eq_u32_e64 s[90:91], 9, v62
	v_cmp_eq_u32_e64 s[92:93], 10, v62
	v_cmp_eq_u32_e64 s[94:95], 11, v62
	v_cndmask_b32_e64 v32, 0, v61, s[72:73]
	v_cndmask_b32_e64 v33, 0, v61, s[74:75]
	v_cndmask_b32_e64 v34, 0, v61, s[76:77]
	v_cndmask_b32_e64 v35, 0, v61, s[78:79]
	v_cndmask_b32_e64 v36, 0, v61, s[80:81]
	v_cndmask_b32_e64 v37, 0, v61, s[82:83]
	v_cndmask_b32_e64 v38, 0, v61, s[84:85]
	v_cndmask_b32_e64 v39, 0, v61, s[86:87]
	v_cndmask_b32_e64 v40, 0, v61, s[88:89]
	v_cndmask_b32_e64 v41, 0, v61, s[90:91]
	v_cndmask_b32_e64 v42, 0, v61, s[92:93]
	v_cndmask_b32_e64 v43, 0, v61, s[94:95]
	v_cmp_eq_u32_e64 s[72:73], 0, v115
	s_waitcnt lgkmcnt(3)
	v_mfma_f32_32x32x16_f16 v[16:31], v[32:35], v[44:47], 0
	ds_read_b128 v[44:47], v60 offset:16
	s_waitcnt lgkmcnt(3)
	v_mfma_f32_32x32x16_f16 v[16:31], v[32:35], v[48:51], v[16:31]
	ds_read_b128 v[48:51], v60 offset:11632
	s_waitcnt lgkmcnt(3)
	v_mfma_f32_32x32x16_f16 v[16:31], v[32:35], v[52:55], v[16:31]
	ds_read_b128 v[52:55], v60 offset:23248
	s_waitcnt lgkmcnt(3)
	v_mfma_f32_32x32x16_f16 v[16:31], v[32:35], v[56:59], v[16:31]
	ds_read_b128 v[56:59], v60 offset:34864
	s_waitcnt lgkmcnt(3)
	v_mfma_f32_32x32x16_f16 v[16:31], v[36:39], v[44:47], v[16:31]
	ds_read_b128 v[44:47], v60 offset:32
	s_waitcnt lgkmcnt(3)
	v_mfma_f32_32x32x16_f16 v[16:31], v[36:39], v[48:51], v[16:31]
	ds_read_b128 v[48:51], v60 offset:11648
	s_waitcnt lgkmcnt(3)
	v_mfma_f32_32x32x16_f16 v[16:31], v[36:39], v[52:55], v[16:31]
	ds_read_b128 v[52:55], v60 offset:23264
	s_waitcnt lgkmcnt(3)
	v_mfma_f32_32x32x16_f16 v[16:31], v[36:39], v[56:59], v[16:31]
	ds_read_b128 v[56:59], v60 offset:34880
	s_waitcnt lgkmcnt(3)
	v_mfma_f32_32x32x16_f16 v[16:31], v[40:43], v[44:47], v[16:31]
	s_waitcnt lgkmcnt(2)
	v_mfma_f32_32x32x16_f16 v[16:31], v[40:43], v[48:51], v[16:31]
	s_waitcnt lgkmcnt(1)
	v_mfma_f32_32x32x16_f16 v[16:31], v[40:43], v[52:55], v[16:31]
	s_waitcnt lgkmcnt(0)
	v_mfma_f32_32x32x16_f16 v[16:31], v[40:43], v[56:59], v[16:31]
	s_waitcnt vmcnt(0)
	v_cndmask_b32_e64 v72, v75, v72, s[72:73]
	v_cndmask_b32_e64 v84, v87, v84, s[72:73]
	v_fmac_f32_e32 v64, v14, v76
	v_fmac_f32_e32 v65, v14, v77
	v_fmac_f32_e32 v66, v14, v78
	v_fmac_f32_e32 v67, v14, v79
	v_fmac_f32_e32 v68, v14, v80
	v_fmac_f32_e32 v69, v14, v81
	v_fmac_f32_e32 v70, v14, v82
	v_fmac_f32_e32 v71, v14, v83
	v_fmac_f32_e32 v72, v14, v84
	v_fmac_f32_e32 v73, v14, v85
	v_fmac_f32_e32 v74, v14, v86
	v_fmac_f32_e32 v75, v14, v87
	v_add_f32_e32 v16, v88, v16
	v_max_f32_e32 v16, 0, v16
	v_fmac_f32_e32 v64, v16, v12
	v_mul_f32_e32 v64, v13, v64
	v_add_f32_e32 v17, v89, v17
	v_max_f32_e32 v17, 0, v17
	v_fmac_f32_e32 v65, v17, v12
	v_mul_f32_e32 v65, v13, v65
	v_add_f32_e32 v18, v90, v18
	v_max_f32_e32 v18, 0, v18
	v_fmac_f32_e32 v66, v18, v12
	v_mul_f32_e32 v66, v13, v66
	v_add_f32_e32 v19, v91, v19
	v_max_f32_e32 v19, 0, v19
	v_fmac_f32_e32 v67, v19, v12
	v_mul_f32_e32 v67, v13, v67
	v_add_f32_e32 v20, v92, v20
	v_max_f32_e32 v20, 0, v20
	v_fmac_f32_e32 v68, v20, v12
	v_mul_f32_e32 v68, v13, v68
	v_add_f32_e32 v21, v93, v21
	v_max_f32_e32 v21, 0, v21
	v_fmac_f32_e32 v69, v21, v12
	v_mul_f32_e32 v69, v13, v69
	v_add_f32_e32 v22, v94, v22
	v_max_f32_e32 v22, 0, v22
	v_fmac_f32_e32 v70, v22, v12
	v_mul_f32_e32 v70, v13, v70
	v_add_f32_e32 v23, v95, v23
	v_max_f32_e32 v23, 0, v23
	v_fmac_f32_e32 v71, v23, v12
	v_mul_f32_e32 v71, v13, v71
	v_add_f32_e32 v24, v96, v24
	v_max_f32_e32 v24, 0, v24
	v_fmac_f32_e32 v72, v24, v12
	v_mul_f32_e32 v72, v13, v72
	v_add_f32_e32 v25, v97, v25
	v_max_f32_e32 v25, 0, v25
	v_fmac_f32_e32 v73, v25, v12
	v_mul_f32_e32 v73, v13, v73
	v_add_f32_e32 v26, v98, v26
	v_max_f32_e32 v26, 0, v26
	v_fmac_f32_e32 v74, v26, v12
	v_mul_f32_e32 v74, v13, v74
	v_add_f32_e32 v27, v99, v27
	v_max_f32_e32 v27, 0, v27
	v_fmac_f32_e32 v75, v27, v12
	v_mul_f32_e32 v75, v13, v75
	v_cndmask_b32_e64 v73, 0, v73, s[72:73]
	v_cndmask_b32_e64 v74, 0, v74, s[72:73]
	v_cndmask_b32_e64 v75, 0, v75, s[72:73]
	v_mul_u32_u24_e32 v10, 0x54, v3
	v_lshl_add_u32 v10, v115, 4, v10
	v_add_u32_e32 v112, 0xb600, v10
	ds_write2_b32 v112, v64, v65 offset1:1
	ds_write2_b32 v112, v66, v67 offset0:2 offset1:3
	ds_write2_b32 v112, v68, v69 offset0:8 offset1:9
	ds_write2_b32 v112, v70, v71 offset0:10 offset1:11
	ds_write_b32 v112, v72 offset:64
	s_mov_b32 exec_hi, 0
	ds_write2_b32 v112, v73, v74 offset0:17 offset1:18
	ds_write_b32 v112, v75 offset:76
	s_mov_b32 exec_hi, -1
	v_add_f32_e32 v28, v64, v65
	v_add_f32_e32 v28, v28, v66
	v_add_f32_e32 v28, v28, v67
	v_add_f32_e32 v28, v28, v68
	v_add_f32_e32 v28, v28, v69
	v_add_f32_e32 v28, v28, v70
	v_add_f32_e32 v28, v28, v71
	v_add_f32_e32 v28, v28, v72
	v_add_f32_e32 v28, v28, v73
	v_add_f32_e32 v28, v28, v74
	v_add_f32_e32 v28, v28, v75
	v_mov_b32_e32 v29, v28
	s_nop 1
	v_permlane32_swap_b32_e32 v28, v29
	v_add_f32_e32 v28, v28, v29
	v_mul_f32_e32 v28, 0x3d430c31, v28
	v_sub_f32_e32 v64, v64, v28
	v_sub_f32_e32 v65, v65, v28
	v_sub_f32_e32 v66, v66, v28
	v_sub_f32_e32 v67, v67, v28
	v_sub_f32_e32 v68, v68, v28
	v_sub_f32_e32 v69, v69, v28
	v_sub_f32_e32 v70, v70, v28
	v_sub_f32_e32 v71, v71, v28
	v_sub_f32_e32 v72, v72, v28
	v_sub_f32_e32 v73, v73, v28
	v_sub_f32_e32 v74, v74, v28
	v_sub_f32_e32 v75, v75, v28
	v_cndmask_b32_e64 v73, 0, v73, s[72:73]
	v_cndmask_b32_e64 v74, 0, v74, s[72:73]
	v_cndmask_b32_e64 v75, 0, v75, s[72:73]
	v_mul_f32_e32 v30, v64, v64
	v_fmac_f32_e32 v30, v65, v65
	v_fmac_f32_e32 v30, v66, v66
	v_fmac_f32_e32 v30, v67, v67
	v_fmac_f32_e32 v30, v68, v68
	v_fmac_f32_e32 v30, v69, v69
	v_fmac_f32_e32 v30, v70, v70
	v_fmac_f32_e32 v30, v71, v71
	v_fmac_f32_e32 v30, v72, v72
	v_fmac_f32_e32 v30, v73, v73
	v_fmac_f32_e32 v30, v74, v74
	v_fmac_f32_e32 v30, v75, v75
	v_mov_b32_e32 v31, v30
	s_nop 1
	v_permlane32_swap_b32_e32 v30, v31
	v_add_f32_e32 v30, v30, v31
	v_mov_b32_e32 v31, 0x3727c5ac
	v_fmac_f32_e32 v31, 0x3d430c31, v30
	v_rsq_f32_e32 v31, v31
	s_nop 0
	v_mul_f32_e32 v31, v13, v31
	v_mul_f32_e32 v64, v64, v31
	v_mul_f32_e32 v116, v13, v116
	v_fmac_f32_e32 v116, v64, v100
	v_mul_f32_e32 v65, v65, v31
	v_mul_f32_e32 v117, v13, v117
	v_fmac_f32_e32 v117, v65, v101
	v_mul_f32_e32 v66, v66, v31
	v_mul_f32_e32 v118, v13, v118
	v_fmac_f32_e32 v118, v66, v102
	v_mul_f32_e32 v67, v67, v31
	v_mul_f32_e32 v119, v13, v119
	v_fmac_f32_e32 v119, v67, v103
	v_mul_f32_e32 v68, v68, v31
	v_mul_f32_e32 v120, v13, v120
	v_fmac_f32_e32 v120, v68, v104
	v_mul_f32_e32 v69, v69, v31
	v_mul_f32_e32 v121, v13, v121
	v_fmac_f32_e32 v121, v69, v105
	v_mul_f32_e32 v70, v70, v31
	v_mul_f32_e32 v122, v13, v122
	v_fmac_f32_e32 v122, v70, v106
	v_mul_f32_e32 v71, v71, v31
	v_mul_f32_e32 v123, v13, v123
	v_fmac_f32_e32 v123, v71, v107
	v_mul_f32_e32 v72, v72, v31
	v_mul_f32_e32 v124, v13, v124
	v_fmac_f32_e32 v124, v72, v108
	v_mul_f32_e32 v73, v73, v31
	v_mul_f32_e32 v125, v13, v125
	v_fmac_f32_e32 v125, v73, v109
	v_mul_f32_e32 v74, v74, v31
	v_mul_f32_e32 v126, v13, v126
	v_fmac_f32_e32 v126, v74, v110
	v_mul_f32_e32 v75, v75, v31
	v_mul_f32_e32 v127, v13, v127
	v_fmac_f32_e32 v127, v75, v111
	v_cndmask_b32_e64 v125, 0, v125, s[72:73]
	v_cndmask_b32_e64 v126, 0, v126, s[72:73]
	v_cndmask_b32_e64 v127, 0, v127, s[72:73]
	v_cvt_pk_f16_f32 v4, v116, v117
	v_cvt_pk_f16_f32 v5, v118, v119
	v_cvt_pk_f16_f32 v6, v120, v121
	v_cvt_pk_f16_f32 v7, v122, v123
	v_cvt_pk_f16_f32 v8, v124, v125
	v_cvt_pk_f16_f32 v9, v126, v127
	v_mul_u32_u24_e32 v10, 0x50, v3
	v_lshl_add_u32 v10, v115, 3, v10
	v_add_u32_e32 v113, 0xf550, v10
	ds_write_b64 v113, v[4:5]
	ds_write_b64 v113, v[6:7] offset:16
	ds_write_b64 v113, v[8:9] offset:32
	v_mov_b32_e32 v28, 0
	v_mov_b32_e32 v29, 0
	v_mov_b32_e32 v30, 0
	v_mov_b32_e32 v31, 0
	s_mov_b32 exec_hi, 0
	ds_write_b128 v113, v[28:31] offset:48
	s_mov_b32 exec_hi, -1

.LBB1_55:
	s_setprio 2
	v_lshrrev_b32_e32 v12, 1, v0
	v_and_b32_e32 v13, 3, v0
	v_and_or_b32 v17, v12, 12, v13
	v_and_b32_e32 v16, 16, v1
	s_lshl_b32 s7, s42, 5
	s_movk_i32 s6, 0x50
	v_or3_b32 v16, v17, v16, s7
	v_mul_lo_u32 v14, v16, s6
	v_add_u32_e32 v16, 0xf550, v14
	v_add_u32_e32 v82, v16, v116
	ds_read_b128 v[38:41], v82
	ds_read_b128 v[110:113], v82 offset:32
	s_movk_i32 s7, 0x500
	s_waitcnt vmcnt(0) lgkmcnt(1)
	v_mfma_f32_32x32x16_f16 v[18:33], v[38:41], v[2:5], 0
	v_mfma_f32_32x32x16_f16 v[2:17], v[38:41], v[6:9], 0
	s_waitcnt lgkmcnt(0)
	v_mfma_f32_32x32x16_f16 v[2:17], v[110:113], v[54:57], v[2:17]
	v_mfma_f32_32x32x16_f16 v[34:49], v[38:41], v[34:37], 0
	v_mfma_f32_32x32x16_f16 v[34:49], v[110:113], v[58:61], v[34:49]
	v_mfma_f32_32x32x16_f16 v[18:33], v[110:113], v[50:53], v[18:33]
	s_nop 5
	v_or_b32_e32 v57, 11, v71
	v_or_b32_e32 v56, 12, v71
	v_or_b32_e32 v55, 13, v71
	v_or_b32_e32 v54, 14, v71
	v_or_b32_e32 v50, 15, v71
	v_add_f32_e32 v34, v83, v34
	v_add_f32_e32 v34, v34, v75
	v_mul_f32_e32 v34, 0xbfb8aa3b, v34
	v_exp_f32_e32 v34, v34
	v_mov_b32_e32 v51, 0xf550
	v_add_f32_e32 v35, v83, v35
	v_lshl_add_u32 v51, v64, 1, v51
	v_mul_lo_u32 v52, v65, s7
	v_add_f32_e32 v35, v35, v76
	v_add_u32_e32 v80, v51, v52
	v_mul_lo_u32 v52, v70, s6
	v_add_f32_e32 v34, 1.0, v34
	v_mul_f32_e32 v35, 0xbfb8aa3b, v35
	v_add_u32_e32 v75, v51, v52
	v_add_u32_e32 v52, 0x1e0, v52
	v_rcp_f32_e32 v34, v34
	v_exp_f32_e32 v76, v35
	v_add_u32_e32 v51, v51, v52
	ds_read_u16 v52, v80
	ds_read_u16 v53, v75
	ds_read_u16 v58, v75 offset:80
	ds_read_u16 v59, v75 offset:160
	ds_read_u16 v60, v75 offset:240
	ds_read_u16 v61, v75 offset:320
	ds_read_u16 v110, v75 offset:400
	ds_read_u16 v111, v51
	s_waitcnt lgkmcnt(7)
	v_cvt_f32_f16_e32 v52, v52
	v_add_f32_e32 v18, v81, v18
	v_add_f32_e32 v36, v83, v36
	v_mul_f32_e32 v35, v72, v34
	v_mul_f32_e32 v18, v18, v34
	v_add_f32_e32 v34, 1.0, v76
	s_waitcnt vmcnt(27)
	v_add_f32_e32 v36, v36, v105
	v_rcp_f32_e32 v34, v34
	v_mul_f32_e32 v36, 0xbfb8aa3b, v36
	v_mul_f32_e32 v52, v18, v52
	s_waitcnt lgkmcnt(6)
	v_cvt_f32_f16_e32 v18, v53
	v_exp_f32_e32 v36, v36
	v_add_f32_e32 v19, v81, v19
	v_mul_f32_e32 v19, v19, v34
	v_mul_f32_e32 v53, v19, v18
	v_add_f32_e32 v18, 1.0, v36
	v_rcp_f32_e32 v18, v18
	v_add_f32_e32 v36, v83, v37
	s_waitcnt lgkmcnt(5)
	v_cvt_f32_f16_e32 v19, v58
	s_waitcnt vmcnt(25)
	v_add_f32_e32 v36, v36, v106
	v_mul_f32_e32 v36, 0xbfb8aa3b, v36
	v_exp_f32_e32 v36, v36
	v_add_f32_e32 v20, v81, v20
	v_fmac_f32_e32 v52, 0, v35
	v_mul_f32_e32 v72, v74, v34
	v_mul_f32_e32 v34, v77, v18
	v_mul_f32_e32 v18, v20, v18
	v_fmac_f32_e32 v53, v52, v72
	v_mul_f32_e32 v76, v35, v72
	v_mul_f32_e32 v58, v18, v19
	v_fmac_f32_e32 v58, v53, v34
	v_mul_f32_e32 v37, v76, v34
	v_add_f32_e32 v34, v83, v38
	v_add_f32_e32 v18, 1.0, v36
	s_waitcnt vmcnt(23)
	v_add_f32_e32 v34, v34, v107
	v_rcp_f32_e32 v18, v18
	v_mul_f32_e32 v34, 0xbfb8aa3b, v34
	s_waitcnt lgkmcnt(4)
	v_cvt_f32_f16_e32 v19, v59
	v_exp_f32_e32 v34, v34
	v_add_f32_e32 v21, v81, v21
	v_mul_f32_e32 v20, v78, v18
	v_mul_f32_e32 v18, v21, v18
	v_add_f32_e32 v21, v83, v39
	v_mul_f32_e32 v59, v18, v19
	v_add_f32_e32 v18, 1.0, v34
	s_waitcnt vmcnt(21)
	v_add_f32_e32 v21, v21, v108
	v_rcp_f32_e32 v18, v18
	v_mul_f32_e32 v21, 0xbfb8aa3b, v21
	s_waitcnt lgkmcnt(3)
	v_cvt_f32_f16_e32 v19, v60
	v_exp_f32_e32 v21, v21
	v_add_f32_e32 v22, v81, v22
	v_fmac_f32_e32 v59, v58, v20
	v_mul_f32_e32 v77, v37, v20
	v_mul_f32_e32 v20, v79, v18
	v_mul_f32_e32 v18, v22, v18
	v_mul_f32_e32 v60, v18, v19
	v_add_f32_e32 v18, 1.0, v21
	v_add_f32_e32 v21, v83, v40
	s_waitcnt vmcnt(19)
	v_add_f32_e32 v21, v21, v109
	v_rcp_f32_e32 v18, v18
	v_mul_f32_e32 v21, 0xbfb8aa3b, v21
	s_waitcnt lgkmcnt(2)
	v_cvt_f32_f16_e32 v19, v61
	v_exp_f32_e32 v21, v21
	v_add_f32_e32 v22, v81, v23
	v_fmac_f32_e32 v60, v59, v20
	v_mul_f32_e32 v39, v77, v20
	v_mul_f32_e32 v20, v102, v18
	v_mul_f32_e32 v18, v22, v18
	v_mul_f32_e32 v61, v18, v19
	v_add_f32_e32 v18, 1.0, v21
	v_add_f32_e32 v21, v83, v41
	s_waitcnt vmcnt(17)
	v_add_f32_e32 v21, v21, v104
	v_rcp_f32_e32 v18, v18
	v_mul_f32_e32 v21, 0xbfb8aa3b, v21
	s_waitcnt lgkmcnt(1)
	v_cvt_f32_f16_e32 v19, v110
	v_exp_f32_e32 v21, v21
	v_add_f32_e32 v22, v81, v24
	v_fmac_f32_e32 v61, v60, v20
	v_mul_f32_e32 v78, v39, v20
	v_mul_f32_e32 v20, v103, v18
	v_mul_f32_e32 v18, v22, v18
	v_mul_f32_e32 v72, v18, v19
	v_add_f32_e32 v18, 1.0, v21
	v_rcp_f32_e32 v18, v18
	v_add_f32_e32 v21, v81, v25
	v_fmac_f32_e32 v72, v61, v20
	v_mul_f32_e32 v79, v78, v20
	s_waitcnt vmcnt(16)
	v_mul_f32_e32 v20, v101, v18
	v_mul_f32_e32 v18, v21, v18
	v_add_f32_e32 v21, v83, v42
	s_waitcnt vmcnt(15)
	v_add_f32_e32 v21, v21, v100
	v_mul_f32_e32 v21, 0xbfb8aa3b, v21
	s_waitcnt lgkmcnt(0)
	v_cvt_f32_f16_e32 v19, v111
	v_exp_f32_e32 v21, v21
	v_add_f32_e32 v36, v83, v43
	v_mul_f32_e32 v41, v79, v20
	v_mul_f32_e32 v74, v18, v19
	v_add_f32_e32 v18, 1.0, v21
	v_fmac_f32_e32 v74, v72, v20
	v_rcp_f32_e32 v18, v18
	ds_read_u16 v19, v51 offset:80
	ds_read_u16 v20, v51 offset:160
	ds_read_u16 v21, v51 offset:240
	ds_read_u16 v22, v51 offset:320
	ds_read_u16 v23, v51 offset:400
	ds_read_u16 v24, v51 offset:480
	ds_read_u16 v25, v51 offset:560
	ds_read_u16 v42, v51 offset:640
	s_waitcnt vmcnt(13)
	v_add_f32_e32 v36, v36, v98
	s_waitcnt lgkmcnt(7)
	v_cvt_f32_f16_e32 v19, v19
	v_mul_f32_e32 v36, 0xbfb8aa3b, v36
	v_exp_f32_e32 v36, v36
	v_add_f32_e32 v26, v81, v26
	v_mul_f32_e32 v34, v84, v18
	v_mul_f32_e32 v18, v26, v18
	v_mul_f32_e32 v26, v18, v19
	v_add_f32_e32 v18, 1.0, v36
	v_fmac_f32_e32 v26, v74, v34
	v_mul_f32_e32 v84, v41, v34
	v_add_f32_e32 v34, v83, v44
	v_rcp_f32_e32 v18, v18
	s_waitcnt vmcnt(11)
	v_add_f32_e32 v34, v34, v97
	s_waitcnt lgkmcnt(6)
	v_cvt_f32_f16_e32 v19, v20
	v_mul_f32_e32 v34, 0xbfb8aa3b, v34
	v_exp_f32_e32 v36, v34
	v_add_f32_e32 v27, v81, v27
	v_mul_f32_e32 v20, v85, v18
	v_mul_f32_e32 v18, v27, v18
	v_mul_f32_e32 v34, v18, v19
	s_waitcnt lgkmcnt(5)
	v_cvt_f32_f16_e32 v19, v21
	v_add_f32_e32 v21, v83, v45
	v_add_f32_e32 v18, 1.0, v36
	s_waitcnt vmcnt(9)
	v_add_f32_e32 v21, v21, v96
	v_rcp_f32_e32 v18, v18
	v_mul_f32_e32 v21, 0xbfb8aa3b, v21
	v_exp_f32_e32 v21, v21
	v_add_f32_e32 v27, v81, v28
	v_fmac_f32_e32 v34, v26, v20
	v_mul_f32_e32 v85, v84, v20
	v_mul_f32_e32 v20, v86, v18
	v_mul_f32_e32 v18, v27, v18
	v_mul_f32_e32 v28, v18, v19
	v_add_f32_e32 v18, 1.0, v21
	v_add_f32_e32 v21, v83, v46
	s_waitcnt vmcnt(7)
	v_add_f32_e32 v21, v21, v95
	v_rcp_f32_e32 v18, v18
	v_mul_f32_e32 v21, 0xbfb8aa3b, v21
	s_waitcnt lgkmcnt(4)
	v_cvt_f32_f16_e32 v19, v22
	v_exp_f32_e32 v21, v21
	v_add_f32_e32 v22, v81, v29
	v_fmac_f32_e32 v28, v34, v20
	v_mul_f32_e32 v86, v85, v20
	v_mul_f32_e32 v20, v87, v18
	v_mul_f32_e32 v18, v22, v18
	v_mul_f32_e32 v36, v18, v19
	v_add_f32_e32 v18, 1.0, v21
	v_add_f32_e32 v21, v83, v47
	s_waitcnt vmcnt(5)
	v_add_f32_e32 v21, v21, v93
	v_rcp_f32_e32 v18, v18
	v_mul_f32_e32 v21, 0xbfb8aa3b, v21
	s_waitcnt lgkmcnt(3)
	v_cvt_f32_f16_e32 v19, v23
	v_exp_f32_e32 v21, v21
	v_add_f32_e32 v22, v81, v30
	v_fmac_f32_e32 v36, v28, v20
	v_mul_f32_e32 v87, v86, v20
	v_mul_f32_e32 v20, v92, v18
	v_mul_f32_e32 v18, v22, v18
	v_mul_f32_e32 v38, v18, v19
	v_add_f32_e32 v18, 1.0, v21
	v_add_f32_e32 v21, v83, v48
	s_waitcnt vmcnt(3)
	v_add_f32_e32 v21, v21, v94
	v_rcp_f32_e32 v18, v18
	v_mul_f32_e32 v21, 0xbfb8aa3b, v21
	s_waitcnt lgkmcnt(2)
	v_cvt_f32_f16_e32 v19, v24
	v_exp_f32_e32 v21, v21
	v_add_f32_e32 v22, v81, v31
	v_fmac_f32_e32 v38, v36, v20
	v_mul_f32_e32 v47, v87, v20
	v_mul_f32_e32 v20, v89, v18
	v_mul_f32_e32 v18, v22, v18
	v_mul_f32_e32 v40, v18, v19
	v_add_f32_e32 v18, 1.0, v21
	v_add_f32_e32 v21, v83, v49
	s_waitcnt vmcnt(1)
	v_add_f32_e32 v21, v21, v91
	v_rcp_f32_e32 v18, v18
	v_mul_f32_e32 v21, 0xbfb8aa3b, v21
	s_waitcnt lgkmcnt(1)
	v_cvt_f32_f16_e32 v19, v25
	v_exp_f32_e32 v21, v21
	v_add_f32_e32 v22, v81, v32
	v_fmac_f32_e32 v40, v38, v20
	v_mul_f32_e32 v31, v47, v20
	v_mul_f32_e32 v20, v90, v18
	v_mul_f32_e32 v18, v22, v18
	v_mul_f32_e32 v32, v18, v19
	v_add_f32_e32 v18, 1.0, v21
	v_rcp_f32_e32 v18, v18
	s_waitcnt lgkmcnt(0)
	v_cvt_f32_f16_e32 v19, v42
	v_add_f32_e32 v21, v81, v33
	v_fmac_f32_e32 v32, v40, v20
	v_mul_f32_e32 v48, v31, v20
	s_waitcnt vmcnt(0)
	v_mul_f32_e32 v20, v88, v18
	v_mul_f32_e32 v18, v21, v18
	v_mul_f32_e32 v30, v18, v19
	v_fmac_f32_e32 v30, v32, v20
	v_mul_f32_e32 v49, v48, v20
	s_and_saveexec_b64 s[6:7], s[0:1]
	s_cbranch_execz .LBB1_57
	v_add_f32_e32 v2, 0, v2
	v_add_f32_e32 v2, v2, v3
	v_add_f32_e32 v2, v2, v4
	v_add_f32_e32 v2, v2, v5
	v_add_f32_e32 v2, v2, v6
	v_add_f32_e32 v2, v2, v7
	v_add_f32_e32 v2, v2, v8
	v_add_f32_e32 v2, v2, v9
	v_add_f32_e32 v2, v2, v10
	v_add_f32_e32 v2, v2, v11
	v_add_f32_e32 v2, v2, v12
	v_add_f32_e32 v2, v2, v13
	v_add_f32_e32 v2, v2, v14
	v_mul_lo_u32 v3, v65, 21
	v_add_f32_e32 v2, v2, v15
	v_add_lshl_u32 v3, v3, v114, 2
	v_add_f32_e32 v2, v2, v16
	v_add_u32_e32 v4, 0x12450, v3
	v_add_f32_e32 v2, v2, v17
	ds_write_b32 v4, v49
	v_add_u32_e32 v4, 0x126f0, v3
	v_add_u32_e32 v3, 0x12990, v3
	ds_write_b32 v4, v30
	ds_write_b32 v3, v2
